# speedup vs baseline: 1.0069x; 1.0069x over previous
_Z8dog_mainPKfS0_S0_S0_S0_S0_S0_Pf:
	s_load_dwordx8 s[12:19], s[0:1], 0x0
	s_load_dwordx8 s[20:27], s[0:1], 0x20
	s_and_b32 s3, s2, 7
	s_lshl_b32 s3, s3, 5
	s_lshr_b32 s4, s2, 3
	s_add_i32 s4, s3, s4
	s_and_b32 s6, s4, 3
	s_lshr_b32 s7, s4, 2
	s_mov_b32 s5, 0
	s_lshl_b64 s[8:9], s[4:5], 18
	v_and_b32_e32 v1, 63, v0
	v_lshrrev_b32_e32 v2, 6, v0
	v_and_b32_e32 v3, 15, v0
	v_and_b32_e32 v7, 31, v0
	v_lshl_or_b32 v5, v2, 5, v7
	v_lshlrev_b32_e32 v5, 2, v5
	v_mov_b32_e32 v4, v5
	v_lshlrev_b32_e32 v6, 4, v1
	v_lshl_or_b32 v6, v2, 12, v6
	v_bfe_u32 v7, v0, 4, 2
	v_readfirstlane_b32 s28, v2
	s_waitcnt lgkmcnt(0)
	global_load_dword v32, v4, s[18:19]
	global_load_dword v33, v4, s[20:21]
	global_load_dword v34, v4, s[22:23]
	global_load_dword v35, v4, s[24:25]
	global_load_dword v36, v4, s[14:15]
	global_load_dword v37, v4, s[16:17]
	s_add_u32 s12, s12, s8
	s_addc_u32 s13, s13, s9
	global_load_dwordx4 v[128:131], v6, s[12:13] offset:0 nt
	global_load_dwordx4 v[132:135], v6, s[12:13] offset:1024 nt
	global_load_dwordx4 v[136:139], v6, s[12:13] offset:2048 nt
	global_load_dwordx4 v[140:143], v6, s[12:13] offset:3072 nt
	v_add_u32_e32 v6, 0x8000, v6
	global_load_dwordx4 v[144:147], v6, s[12:13] offset:0 nt
	global_load_dwordx4 v[148:151], v6, s[12:13] offset:1024 nt
	global_load_dwordx4 v[152:155], v6, s[12:13] offset:2048 nt
	global_load_dwordx4 v[156:159], v6, s[12:13] offset:3072 nt
	s_cmp_ge_u32 s28, 4
	s_cbranch_scc0 .Lstag_skip
	s_sleep 8
.Lstag_skip:
	v_and_b32_e32 v16, 1, v0
	v_cmp_eq_u32_e64 s[30:31], 0, v16
	v_and_b32_e32 v17, 2, v0
	v_cmp_eq_u32_e64 s[32:33], 0, v17
	v_and_b32_e32 v16, 3, v0
	v_lshrrev_b32_e32 v17, 2, v1
	v_lshlrev_b32_e32 v16, 5, v16
	v_lshl_add_u32 v16, v17, 1, v16
	v_lshrrev_b32_e32 v17, 1, v2
	s_movk_i32 s10, 0x110
	v_mad_u32_u24 v16, v17, s10, v16
	v_and_b32_e32 v17, 1, v2
	v_lshl_add_u32 v14, v17, 7, v16
	v_lshlrev_b32_e32 v17, 4, v7
	v_mad_u32_u24 v15, v3, s10, v17
	s_lshl_b32 s11, s6, 5
	v_lshl_add_u32 v18, v7, 2, s11
	v_cvt_f32_u32_e32 v18, v18
	v_lshlrev_b32_e32 v19, 3, v7
	v_cvt_f32_u32_e32 v19, v19
	s_waitcnt vmcnt(8)
	v_lshlrev_b32_e32 v16, 2, v3
	v_add_u32_e32 v17, 64, v16
	ds_bpermute_b32 v40, v16, v32
	ds_bpermute_b32 v46, v17, v32
	ds_bpermute_b32 v41, v16, v33
	ds_bpermute_b32 v47, v17, v33
	ds_bpermute_b32 v42, v16, v34
	ds_bpermute_b32 v48, v17, v34
	ds_bpermute_b32 v43, v16, v35
	ds_bpermute_b32 v49, v17, v35
	ds_bpermute_b32 v44, v16, v36
	ds_bpermute_b32 v50, v17, v36
	ds_bpermute_b32 v45, v16, v37
	ds_bpermute_b32 v51, v17, v37
	s_waitcnt lgkmcnt(0)
	v_add_f32_e32 v41, v40, v41
	v_sub_f32_e32 v12, v19, v42
	v_sub_f32_e32 v13, v18, v43
	v_rcp_f32_e32 v42, v40
	v_rcp_f32_e32 v43, v41
	s_nop 0
	v_fma_f32 v20, -v40, v42, 1.0
	v_fma_f32 v42, v20, v42, v42
	v_fma_f32 v20, -v41, v43, 1.0
	v_fma_f32 v43, v20, v43, v43
	v_mul_f32_e32 v8, 0xbf38aa3b, v42
	v_mul_f32_e32 v9, 0xbf38aa3b, v43
	v_mul_f32_e32 v44, v44, v42
	v_mul_f32_e32 v45, v45, v43
	v_mul_f32_e32 v10, 0x3e22f983, v44
	v_mul_f32_e32 v11, 0x3e22f983, v45
	v_add_f32_e32 v47, v46, v47
	v_sub_f32_e32 v2, v19, v48
	v_sub_f32_e32 v3, v18, v49
	v_rcp_f32_e32 v48, v46
	v_rcp_f32_e32 v49, v47
	s_nop 0
	v_fma_f32 v20, -v46, v48, 1.0
	v_fma_f32 v48, v20, v48, v48
	v_fma_f32 v20, -v47, v49, 1.0
	v_fma_f32 v49, v20, v49, v49
	v_mul_f32_e32 v28, 0xbf38aa3b, v48
	v_mul_f32_e32 v29, 0xbf38aa3b, v49
	v_mul_f32_e32 v50, v50, v48
	v_mul_f32_e32 v51, v51, v49
	v_mul_f32_e32 v30, 0x3e22f983, v50
	v_mul_f32_e32 v31, 0x3e22f983, v51
	s_getpc_b64 s[44:45]
